# speedup vs baseline: 1.0210x; 1.0210x over previous
.LBB1_2:
	v_or_b32_e32 v118, 0x14000, v1
	v_mov_b32_e32 v99, 0
	s_bfe_u32 s40, s19, 0x20006
	s_waitcnt vmcnt(4)
	s_barrier
	s_mov_b64 s[20:21], 0x80
	s_add_u32 s58, s2, s20
	s_addc_u32 s59, s3, s21
	v_readfirstlane_b32 s19, v118
	s_mov_b32 m0, s19
	v_or_b32_e32 v119, 0x16000, v1
	global_load_lds_dwordx4 v100, s[58:59]
	v_readfirstlane_b32 s19, v119
	s_add_u32 s58, s2, s20
	s_addc_u32 s59, s3, s21
	s_mov_b32 m0, s19
	v_or_b32_e32 v120, 0x6000, v1
	global_load_lds_dwordx4 v103, s[58:59]
	v_readfirstlane_b32 s19, v120
	s_add_u32 s58, s16, s20
	s_addc_u32 s59, s17, s21
	v_or_b32_e32 v3, 0x8000, v1
	s_mov_b32 m0, s19
	v_cndmask_b32_e32 v121, v2, v3, vcc
	global_load_lds_dwordx4 v100, s[58:59]
	v_readfirstlane_b32 s19, v121
	s_add_u32 s58, s16, s20
	s_addc_u32 s59, s17, s21
	v_or_b32_e32 v123, 0x18000, v1
	s_mov_b32 m0, s19
	s_add_u32 s20, s2, 0x40080
	v_mov_b32_e32 v3, v100
	v_readfirstlane_b32 s22, v123
	v_or_b32_e32 v124, 0x1a000, v1
	global_load_lds_dwordx4 v101, s[58:59]
	s_addc_u32 s21, s3, 0
	s_mov_b32 m0, s22
	v_readfirstlane_b32 s22, v124
	global_load_lds_dwordx4 v3, s[20:21]
	v_mov_b32_e32 v3, v103
	s_mov_b32 m0, s22
	v_lshlrev_b32_e32 v4, 6, v0
	global_load_lds_dwordx4 v3, s[20:21]
	v_and_b32_e32 v105, 15, v0
	v_and_b32_e32 v3, 48, v0
	v_and_b32_e32 v4, 0x3c0, v4
	v_lshlrev_b32_e32 v6, 2, v0
	s_mul_i32 s37, s18, 48
	s_mov_b32 s1, 0x14000
	s_mov_b32 s19, 0x18000
	s_waitcnt vmcnt(6)
	v_or_b32_e32 v5, v4, v3
	v_and_b32_e32 v6, 32, v6
	v_lshlrev_b32_e32 v10, 6, v105
	s_add_i32 s39, s37, 16
	s_add_i32 s38, s37, 32
	s_lshl_b32 s26, s40, 12
	v_bitop3_b32 v4, v4, v6, v3 bitop3:0x36
	v_add_u32_e32 v7, 0xb000, v1
	v_bitop3_b32 v8, v5, s0, v6 bitop3:0xde
	v_bitop3_b32 v9, v5, s1, v6 bitop3:0xde
	v_bitop3_b32 v5, v5, s19, v6 bitop3:0xde
	v_bitop3_b32 v3, v10, v6, v3 bitop3:0x36
	s_mulk_i32 s18, 0x1800
	s_lshl_b32 s19, s39, 7
	s_lshl_b32 s20, s38, 7
	v_lshrrev_b32_e32 v102, 2, v0
	v_cndmask_b32_e32 v125, v2, v7, vcc
	s_mov_b32 s41, -2
	s_mov_b64 s[0:1], 0
	v_add_u32_e32 v126, s26, v4
	v_add_u32_e32 v110, s18, v3
	v_add_u32_e32 v109, s19, v4
	v_add_u32_e32 v108, s20, v4
	s_mov_b64 s[18:19], 0x30080
	v_add_u32_e32 v127, 0x9000, v1
	v_add_u32_e32 v122, s26, v8
	s_mov_b64 s[20:21], 0x100
	s_mov_b64 s[22:23], 0x40100
	v_add_u32_e32 v117, s26, v9
	s_mov_b64 s[24:25], 0x30100
	v_add_u32_e32 v114, s26, v5
	s_mov_b64 s[26:27], 0x180
	s_mov_b64 s[28:29], 0x40180
	v_mov_b32_e32 v2, v99
	v_mov_b32_e32 v3, v99
	v_mov_b32_e32 v4, v99
	v_mov_b32_e32 v5, v99
	v_mov_b32_e32 v6, v99
	v_mov_b32_e32 v7, v99
	v_mov_b32_e32 v8, v99
	v_mov_b32_e32 v9, v99
	v_mov_b32_e32 v10, v99
	v_mov_b32_e32 v11, v99
	v_mov_b32_e32 v12, v99
	v_mov_b32_e32 v13, v99
	v_mov_b32_e32 v14, v99
	v_mov_b32_e32 v15, v99
	v_mov_b32_e32 v16, v99
	v_mov_b32_e32 v17, v99
	v_mov_b32_e32 v18, v99
	v_mov_b32_e32 v19, v99
	v_mov_b32_e32 v20, v99
	v_mov_b32_e32 v21, v99
	v_mov_b32_e32 v22, v99
	v_mov_b32_e32 v23, v99
	v_mov_b32_e32 v24, v99
	v_mov_b32_e32 v25, v99
	v_mov_b32_e32 v26, v99
	v_mov_b32_e32 v27, v99
	v_mov_b32_e32 v28, v99
	v_mov_b32_e32 v29, v99
	v_mov_b32_e32 v30, v99
	v_mov_b32_e32 v31, v99
	v_mov_b32_e32 v32, v99
	v_mov_b32_e32 v33, v99
	v_mov_b32_e32 v34, v99
	v_mov_b32_e32 v35, v99
	v_mov_b32_e32 v36, v99
	v_mov_b32_e32 v37, v99
	v_mov_b32_e32 v38, v99
	v_mov_b32_e32 v39, v99
	v_mov_b32_e32 v40, v99
	v_mov_b32_e32 v41, v99
	v_mov_b32_e32 v42, v99
	v_mov_b32_e32 v43, v99
	v_mov_b32_e32 v44, v99
	v_mov_b32_e32 v45, v99
	v_mov_b32_e32 v46, v99
	v_mov_b32_e32 v47, v99
	v_mov_b32_e32 v48, v99
	v_mov_b32_e32 v49, v99
	v_mov_b32_e32 v50, v99
	v_mov_b32_e32 v51, v99
	v_mov_b32_e32 v52, v99
	v_mov_b32_e32 v53, v99
	v_mov_b32_e32 v62, v99
	v_mov_b32_e32 v63, v99
	v_mov_b32_e32 v64, v99
	v_mov_b32_e32 v65, v99
	v_mov_b32_e32 v66, v99
	v_mov_b32_e32 v67, v99
	v_mov_b32_e32 v68, v99
	v_mov_b32_e32 v69, v99
	v_mov_b32_e32 v70, v99
	v_mov_b32_e32 v71, v99
	v_mov_b32_e32 v72, v99
	v_mov_b32_e32 v73, v99
	v_mov_b32_e32 v74, v99
	v_mov_b32_e32 v75, v99
	v_mov_b32_e32 v76, v99
	v_mov_b32_e32 v77, v99
	v_mov_b32_e32 v78, v99
	v_mov_b32_e32 v79, v99
	v_mov_b32_e32 v80, v99
	v_mov_b32_e32 v81, v99
	v_mov_b32_e32 v82, v99
	v_mov_b32_e32 v83, v99
	v_mov_b32_e32 v84, v99
	v_mov_b32_e32 v85, v99
	v_mov_b32_e32 v86, v99
	v_mov_b32_e32 v87, v99
	v_mov_b32_e32 v88, v99
	v_mov_b32_e32 v89, v99
	v_mov_b32_e32 v90, v99
	v_mov_b32_e32 v91, v99
	v_mov_b32_e32 v92, v99
	v_mov_b32_e32 v93, v99
	v_mov_b32_e32 v94, v99
	v_mov_b32_e32 v95, v99
	v_mov_b32_e32 v96, v99
	v_mov_b32_e32 v97, v99
	v_mov_b32_e32 v54, v99
	v_mov_b32_e32 v55, v99
	v_mov_b32_e32 v56, v99
	v_mov_b32_e32 v57, v99
	v_mov_b32_e32 v58, v99
	v_mov_b32_e32 v59, v99
	v_mov_b32_e32 v60, v99
	v_mov_b32_e32 v61, v99
	s_barrier
.LBB1_3:
	ds_read_b128 v[128:131], v126 offset:49152
	ds_read_b128 v[132:135], v126 offset:50176
	ds_read_b128 v[136:139], v126 offset:51200
	ds_read_b128 v[140:143], v126 offset:52224
	s_add_u32 s30, s16, s0
	s_addc_u32 s31, s17, s1
	ds_read_b128 v[144:147], v110
	ds_read_b128 v[148:151], v110 offset:1024
	ds_read_b128 v[152:155], v109
	ds_read_b128 v[156:159], v109 offset:1024
	ds_read_b128 v[160:163], v108
	ds_read_b128 v[164:167], v108 offset:1024
	v_readfirstlane_b32 s34, v127
	s_add_u32 s52, s30, s18
	s_addc_u32 s53, s31, s19
	s_mov_b32 m0, s34
	s_nop 0
	global_load_lds_dwordx4 v100, s[52:53]
	v_readfirstlane_b32 s34, v125
	s_add_u32 s52, s30, s18
	s_addc_u32 s53, s31, s19
	s_mov_b32 m0, s34
	s_nop 0
	global_load_lds_dwordx4 v101, s[52:53]
	s_waitcnt lgkmcnt(6)
	s_barrier
	s_waitcnt lgkmcnt(0)
	s_setprio 1
	s_waitcnt lgkmcnt(0)
	v_mfma_f32_16x16x32_f16 v[94:97], v[144:147], v[128:131], v[94:97]
	v_mfma_f32_16x16x32_f16 v[90:93], v[144:147], v[136:139], v[90:93]
	v_mfma_f32_16x16x32_f16 v[86:89], v[152:155], v[128:131], v[86:89]
	v_mfma_f32_16x16x32_f16 v[82:85], v[152:155], v[136:139], v[82:85]
	v_mfma_f32_16x16x32_f16 v[78:81], v[160:163], v[128:131], v[78:81]
	v_mfma_f32_16x16x32_f16 v[74:77], v[160:163], v[136:139], v[74:77]
	v_mfma_f32_16x16x32_f16 v[94:97], v[148:151], v[132:135], v[94:97]
	v_mfma_f32_16x16x32_f16 v[90:93], v[148:151], v[140:143], v[90:93]
	v_mfma_f32_16x16x32_f16 v[86:89], v[156:159], v[132:135], v[86:89]
	v_mfma_f32_16x16x32_f16 v[82:85], v[156:159], v[140:143], v[82:85]
	v_mfma_f32_16x16x32_f16 v[78:81], v[164:167], v[132:135], v[78:81]
	v_mfma_f32_16x16x32_f16 v[74:77], v[164:167], v[140:143], v[74:77]
	s_setprio 0
	s_barrier
	s_add_u32 s34, s2, s0
	s_addc_u32 s35, s3, s1
	ds_read_b128 v[168:171], v122
	ds_read_b128 v[172:175], v122 offset:1024
	ds_read_b128 v[176:179], v122 offset:2048
	ds_read_b128 v[180:183], v122 offset:3072
	v_readfirstlane_b32 s42, v106
	s_add_u32 s54, s34, s20
	s_addc_u32 s55, s35, s21
	s_mov_b32 m0, s42
	s_nop 0
	global_load_lds_dwordx4 v100, s[54:55]
	v_readfirstlane_b32 s42, v107
	s_add_u32 s54, s34, s20
	s_addc_u32 s55, s35, s21
	s_mov_b32 m0, s42
	s_nop 0
	global_load_lds_dwordx4 v103, s[54:55]
	s_barrier
	s_waitcnt lgkmcnt(0)
	s_setprio 1
	s_waitcnt lgkmcnt(0)
	v_mfma_f32_16x16x32_f16 v[70:73], v[144:147], v[168:171], v[70:73]
	v_mfma_f32_16x16x32_f16 v[66:69], v[144:147], v[176:179], v[66:69]
	v_mfma_f32_16x16x32_f16 v[62:65], v[152:155], v[168:171], v[62:65]
	v_mfma_f32_16x16x32_f16 v[50:53], v[152:155], v[176:179], v[50:53]
	v_mfma_f32_16x16x32_f16 v[46:49], v[160:163], v[168:171], v[46:49]
	v_mfma_f32_16x16x32_f16 v[42:45], v[160:163], v[176:179], v[42:45]
	v_mfma_f32_16x16x32_f16 v[70:73], v[148:151], v[172:175], v[70:73]
	v_mfma_f32_16x16x32_f16 v[66:69], v[148:151], v[180:183], v[66:69]
	v_mfma_f32_16x16x32_f16 v[62:65], v[156:159], v[172:175], v[62:65]
	v_mfma_f32_16x16x32_f16 v[50:53], v[156:159], v[180:183], v[50:53]
	v_mfma_f32_16x16x32_f16 v[46:49], v[164:167], v[172:175], v[46:49]
	v_mfma_f32_16x16x32_f16 v[42:45], v[164:167], v[180:183], v[42:45]
	s_setprio 0
	s_barrier
	ds_read_b128 v[144:147], v110 offset:12288
	ds_read_b128 v[148:151], v110 offset:13312
	ds_read_b128 v[152:155], v109 offset:12288
	ds_read_b128 v[156:159], v109 offset:13312
	ds_read_b128 v[160:163], v108 offset:12288
	ds_read_b128 v[164:167], v108 offset:13312
	v_readfirstlane_b32 s42, v1
	s_add_u32 s54, s30, s20
	s_addc_u32 s55, s31, s21
	s_mov_b32 m0, s42
	s_nop 0
	global_load_lds_dwordx4 v100, s[54:55]
	v_readfirstlane_b32 s42, v111
	s_add_u32 s54, s30, s20
	s_addc_u32 s55, s31, s21
	s_mov_b32 m0, s42
	s_nop 0
	global_load_lds_dwordx4 v101, s[54:55]
	s_barrier
	s_waitcnt lgkmcnt(0)
	s_setprio 1
	s_waitcnt lgkmcnt(0)
	v_mfma_f32_16x16x32_f16 v[38:41], v[144:147], v[128:131], v[38:41]
	v_mfma_f32_16x16x32_f16 v[34:37], v[144:147], v[136:139], v[34:37]
	v_mfma_f32_16x16x32_f16 v[30:33], v[152:155], v[128:131], v[30:33]
	v_mfma_f32_16x16x32_f16 v[26:29], v[152:155], v[136:139], v[26:29]
	v_mfma_f32_16x16x32_f16 v[22:25], v[160:163], v[128:131], v[22:25]
	v_mfma_f32_16x16x32_f16 v[18:21], v[160:163], v[136:139], v[18:21]
	v_mfma_f32_16x16x32_f16 v[38:41], v[148:151], v[132:135], v[38:41]
	v_mfma_f32_16x16x32_f16 v[34:37], v[148:151], v[140:143], v[34:37]
	v_mfma_f32_16x16x32_f16 v[30:33], v[156:159], v[132:135], v[30:33]
	v_mfma_f32_16x16x32_f16 v[26:29], v[156:159], v[140:143], v[26:29]
	v_mfma_f32_16x16x32_f16 v[22:25], v[164:167], v[132:135], v[22:25]
	v_mfma_f32_16x16x32_f16 v[18:21], v[164:167], v[140:143], v[18:21]
	s_setprio 0
	s_barrier
	v_readfirstlane_b32 s42, v112
	s_add_u32 s56, s34, s22
	s_addc_u32 s57, s35, s23
	s_mov_b32 m0, s42
	s_nop 0
	global_load_lds_dwordx4 v100, s[56:57]
	v_readfirstlane_b32 s42, v113
	s_add_u32 s56, s34, s22
	s_addc_u32 s57, s35, s23
	s_mov_b32 m0, s42
	s_nop 0
	global_load_lds_dwordx4 v103, s[56:57]
	s_waitcnt vmcnt(6)
	s_barrier
	s_setprio 1
	v_mfma_f32_16x16x32_f16 v[14:17], v[144:147], v[168:171], v[14:17]
	v_mfma_f32_16x16x32_f16 v[10:13], v[144:147], v[176:179], v[10:13]
	v_mfma_f32_16x16x32_f16 v[6:9], v[152:155], v[168:171], v[6:9]
	v_mfma_f32_16x16x32_f16 v[2:5], v[152:155], v[176:179], v[2:5]
	v_mfma_f32_16x16x32_f16 v[54:57], v[160:163], v[168:171], v[54:57]
	v_mfma_f32_16x16x32_f16 v[58:61], v[160:163], v[176:179], v[58:61]
	v_mfma_f32_16x16x32_f16 v[14:17], v[148:151], v[172:175], v[14:17]
	v_mfma_f32_16x16x32_f16 v[10:13], v[148:151], v[180:183], v[10:13]
	v_mfma_f32_16x16x32_f16 v[6:9], v[156:159], v[172:175], v[6:9]
	v_mfma_f32_16x16x32_f16 v[2:5], v[156:159], v[180:183], v[2:5]
	v_mfma_f32_16x16x32_f16 v[54:57], v[164:167], v[172:175], v[54:57]
	v_mfma_f32_16x16x32_f16 v[58:61], v[164:167], v[180:183], v[58:61]
	s_setprio 0
	s_barrier
	ds_read_b128 v[128:131], v117
	ds_read_b128 v[132:135], v117 offset:1024
	ds_read_b128 v[136:139], v117 offset:2048
	ds_read_b128 v[140:143], v117 offset:3072
	ds_read_b128 v[144:147], v110 offset:24576
	ds_read_b128 v[148:151], v110 offset:25600
	ds_read_b128 v[152:155], v109 offset:24576
	ds_read_b128 v[156:159], v109 offset:25600
	ds_read_b128 v[160:163], v108 offset:24576
	ds_read_b128 v[164:167], v108 offset:25600
	v_readfirstlane_b32 s42, v115
	s_add_u32 s52, s30, s24
	s_addc_u32 s53, s31, s25
	s_mov_b32 m0, s42
	s_nop 0
	global_load_lds_dwordx4 v100, s[52:53]
	v_readfirstlane_b32 s42, v116
	s_add_u32 s52, s30, s24
	s_addc_u32 s53, s31, s25
	s_mov_b32 m0, s42
	s_nop 0
	global_load_lds_dwordx4 v101, s[52:53]
	s_waitcnt lgkmcnt(6)
	s_barrier
	s_waitcnt lgkmcnt(0)
	s_setprio 1
	s_waitcnt lgkmcnt(0)
	v_mfma_f32_16x16x32_f16 v[94:97], v[144:147], v[128:131], v[94:97]
	v_mfma_f32_16x16x32_f16 v[90:93], v[144:147], v[136:139], v[90:93]
	v_mfma_f32_16x16x32_f16 v[86:89], v[152:155], v[128:131], v[86:89]
	v_mfma_f32_16x16x32_f16 v[82:85], v[152:155], v[136:139], v[82:85]
	v_mfma_f32_16x16x32_f16 v[78:81], v[160:163], v[128:131], v[78:81]
	v_mfma_f32_16x16x32_f16 v[74:77], v[160:163], v[136:139], v[74:77]
	v_mfma_f32_16x16x32_f16 v[94:97], v[148:151], v[132:135], v[94:97]
	v_mfma_f32_16x16x32_f16 v[90:93], v[148:151], v[140:143], v[90:93]
	v_mfma_f32_16x16x32_f16 v[86:89], v[156:159], v[132:135], v[86:89]
	v_mfma_f32_16x16x32_f16 v[82:85], v[156:159], v[140:143], v[82:85]
	v_mfma_f32_16x16x32_f16 v[78:81], v[164:167], v[132:135], v[78:81]
	v_mfma_f32_16x16x32_f16 v[74:77], v[164:167], v[140:143], v[74:77]
	s_setprio 0
	s_barrier
	ds_read_b128 v[168:171], v114
	ds_read_b128 v[172:175], v114 offset:1024
	ds_read_b128 v[176:179], v114 offset:2048
	ds_read_b128 v[180:183], v114 offset:3072
	v_readfirstlane_b32 s42, v118
	s_add_u32 s54, s34, s26
	s_addc_u32 s55, s35, s27
	s_mov_b32 m0, s42
	s_nop 0
	global_load_lds_dwordx4 v100, s[54:55]
	v_readfirstlane_b32 s42, v119
	s_add_u32 s54, s34, s26
	s_addc_u32 s55, s35, s27
	s_mov_b32 m0, s42
	s_nop 0
	global_load_lds_dwordx4 v103, s[54:55]
	s_barrier
	s_waitcnt lgkmcnt(0)
	s_setprio 1
	s_waitcnt lgkmcnt(0)
	v_mfma_f32_16x16x32_f16 v[70:73], v[144:147], v[168:171], v[70:73]
	v_mfma_f32_16x16x32_f16 v[66:69], v[144:147], v[176:179], v[66:69]
	v_mfma_f32_16x16x32_f16 v[62:65], v[152:155], v[168:171], v[62:65]
	v_mfma_f32_16x16x32_f16 v[50:53], v[152:155], v[176:179], v[50:53]
	v_mfma_f32_16x16x32_f16 v[46:49], v[160:163], v[168:171], v[46:49]
	v_mfma_f32_16x16x32_f16 v[42:45], v[160:163], v[176:179], v[42:45]
	v_mfma_f32_16x16x32_f16 v[70:73], v[148:151], v[172:175], v[70:73]
	v_mfma_f32_16x16x32_f16 v[66:69], v[148:151], v[180:183], v[66:69]
	v_mfma_f32_16x16x32_f16 v[62:65], v[156:159], v[172:175], v[62:65]
	v_mfma_f32_16x16x32_f16 v[50:53], v[156:159], v[180:183], v[50:53]
	v_mfma_f32_16x16x32_f16 v[46:49], v[164:167], v[172:175], v[46:49]
	v_mfma_f32_16x16x32_f16 v[42:45], v[164:167], v[180:183], v[42:45]
	s_setprio 0
	s_barrier
	ds_read_b128 v[144:147], v110 offset:36864
	ds_read_b128 v[148:151], v110 offset:37888
	ds_read_b128 v[152:155], v109 offset:36864
	ds_read_b128 v[156:159], v109 offset:37888
	ds_read_b128 v[160:163], v108 offset:36864
	ds_read_b128 v[164:167], v108 offset:37888
	v_readfirstlane_b32 s42, v120
	s_add_u32 s54, s30, s26
	s_addc_u32 s55, s31, s27
	s_mov_b32 m0, s42
	s_nop 0
	global_load_lds_dwordx4 v100, s[54:55]
	s_nop 0
	s_add_u32 s54, s30, s26
	s_addc_u32 s55, s31, s27
	v_readfirstlane_b32 s30, v121
	s_mov_b32 m0, s30
	s_nop 0
	global_load_lds_dwordx4 v101, s[54:55]
	s_barrier
	s_waitcnt lgkmcnt(0)
	s_setprio 1
	s_waitcnt lgkmcnt(0)
	v_mfma_f32_16x16x32_f16 v[38:41], v[144:147], v[128:131], v[38:41]
	v_mfma_f32_16x16x32_f16 v[34:37], v[144:147], v[136:139], v[34:37]
	v_mfma_f32_16x16x32_f16 v[30:33], v[152:155], v[128:131], v[30:33]
	v_mfma_f32_16x16x32_f16 v[26:29], v[152:155], v[136:139], v[26:29]
	v_mfma_f32_16x16x32_f16 v[22:25], v[160:163], v[128:131], v[22:25]
	v_mfma_f32_16x16x32_f16 v[18:21], v[160:163], v[136:139], v[18:21]
	v_mfma_f32_16x16x32_f16 v[38:41], v[148:151], v[132:135], v[38:41]
	v_mfma_f32_16x16x32_f16 v[34:37], v[148:151], v[140:143], v[34:37]
	v_mfma_f32_16x16x32_f16 v[30:33], v[156:159], v[132:135], v[30:33]
	v_mfma_f32_16x16x32_f16 v[26:29], v[156:159], v[140:143], v[26:29]
	v_mfma_f32_16x16x32_f16 v[22:25], v[164:167], v[132:135], v[22:25]
	v_mfma_f32_16x16x32_f16 v[18:21], v[164:167], v[140:143], v[18:21]
	s_setprio 0
	s_barrier
	v_readfirstlane_b32 s30, v123
	s_add_u32 s56, s34, s28
	s_addc_u32 s57, s35, s29
	s_mov_b32 m0, s30
	s_nop 0
	global_load_lds_dwordx4 v100, s[56:57]
	v_readfirstlane_b32 s30, v124
	s_add_u32 s56, s34, s28
	s_addc_u32 s57, s35, s29
	s_mov_b32 m0, s30
	s_nop 0
	global_load_lds_dwordx4 v103, s[56:57]
	s_waitcnt vmcnt(6)
	s_barrier
	s_setprio 1
	v_mfma_f32_16x16x32_f16 v[14:17], v[144:147], v[168:171], v[14:17]
	v_mfma_f32_16x16x32_f16 v[10:13], v[144:147], v[176:179], v[10:13]
	v_mfma_f32_16x16x32_f16 v[6:9], v[152:155], v[168:171], v[6:9]
	v_mfma_f32_16x16x32_f16 v[2:5], v[152:155], v[176:179], v[2:5]
	v_mfma_f32_16x16x32_f16 v[54:57], v[160:163], v[168:171], v[54:57]
	v_mfma_f32_16x16x32_f16 v[58:61], v[160:163], v[176:179], v[58:61]
	v_mfma_f32_16x16x32_f16 v[14:17], v[148:151], v[172:175], v[14:17]
	v_mfma_f32_16x16x32_f16 v[10:13], v[148:151], v[180:183], v[10:13]
	v_mfma_f32_16x16x32_f16 v[6:9], v[156:159], v[172:175], v[6:9]
	v_mfma_f32_16x16x32_f16 v[2:5], v[156:159], v[180:183], v[2:5]
	v_mfma_f32_16x16x32_f16 v[54:57], v[164:167], v[172:175], v[54:57]
	v_mfma_f32_16x16x32_f16 v[58:61], v[164:167], v[180:183], v[58:61]
	s_setprio 0
	s_add_i32 s41, s41, 2
	s_add_u32 s0, s0, 0x100
	s_addc_u32 s1, s1, 0
	s_cmp_lt_u32 s41, 12
	s_barrier
	s_cbranch_scc1 .LBB1_3
	v_add_u32_e32 v98, 0x9000, v1
	s_add_u32 s0, s16, 0x30780
	v_readfirstlane_b32 s2, v98
	s_addc_u32 s1, s17, 0
	s_mov_b32 m0, s2
	v_readfirstlane_b32 s2, v125
	ds_read_b128 v[118:121], v126 offset:49152
	ds_read_b128 v[128:131], v126 offset:50176
	ds_read_b128 v[132:135], v126 offset:51200
	ds_read_b128 v[136:139], v126 offset:52224
	ds_read_b128 v[140:143], v110
	ds_read_b128 v[144:147], v110 offset:1024
	ds_read_b128 v[148:151], v109
	ds_read_b128 v[152:155], v109 offset:1024
	ds_read_b128 v[156:159], v108
	ds_read_b128 v[160:163], v108 offset:1024
	s_nop 0
	global_load_lds_dwordx4 v100, s[0:1]
	s_mov_b32 m0, s2
	s_nop 0
	global_load_lds_dwordx4 v101, s[0:1]
	s_barrier
	s_waitcnt lgkmcnt(0)
	s_setprio 1
	s_waitcnt lgkmcnt(0)
	v_mfma_f32_16x16x32_f16 v[90:93], v[140:143], v[132:135], v[90:93]
	v_mfma_f32_16x16x32_f16 v[86:89], v[148:151], v[118:121], v[86:89]
	v_mfma_f32_16x16x32_f16 v[82:85], v[148:151], v[132:135], v[82:85]
	v_mfma_f32_16x16x32_f16 v[94:97], v[140:143], v[118:121], v[94:97]
	v_mfma_f32_16x16x32_f16 v[90:93], v[144:147], v[136:139], v[90:93]
	v_mfma_f32_16x16x32_f16 v[86:89], v[152:155], v[128:131], v[86:89]
	v_mfma_f32_16x16x32_f16 v[82:85], v[152:155], v[136:139], v[82:85]
	v_mfma_f32_16x16x32_f16 v[78:81], v[156:159], v[118:121], v[78:81]
	v_mfma_f32_16x16x32_f16 v[74:77], v[156:159], v[132:135], v[74:77]
	v_mfma_f32_16x16x32_f16 v[94:97], v[144:147], v[128:131], v[94:97]
	v_mfma_f32_16x16x32_f16 v[124:127], v[160:163], v[128:131], v[78:81]
	v_mfma_f32_16x16x32_f16 v[164:167], v[160:163], v[136:139], v[74:77]
	s_setprio 0
	s_barrier
	s_nop 2
	ds_read_b128 v[74:77], v122
	ds_read_b128 v[78:81], v122 offset:1024
	ds_read_b128 v[98:101], v122 offset:2048
	ds_read_b128 v[168:171], v122 offset:3072
	s_barrier
	s_waitcnt lgkmcnt(0)
	s_setprio 1
	s_waitcnt lgkmcnt(0)
	v_mfma_f32_16x16x32_f16 v[70:73], v[140:143], v[74:77], v[70:73]
	v_mfma_f32_16x16x32_f16 v[66:69], v[140:143], v[98:101], v[66:69]
	v_mfma_f32_16x16x32_f16 v[50:53], v[148:151], v[98:101], v[50:53]
	v_mfma_f32_16x16x32_f16 v[46:49], v[156:159], v[74:77], v[46:49]
	v_mfma_f32_16x16x32_f16 v[42:45], v[156:159], v[98:101], v[42:45]
	v_mfma_f32_16x16x32_f16 v[70:73], v[144:147], v[78:81], v[70:73]
	v_mfma_f32_16x16x32_f16 v[66:69], v[144:147], v[168:171], v[66:69]
	v_mfma_f32_16x16x32_f16 v[62:65], v[148:151], v[74:77], v[62:65]
	v_mfma_f32_16x16x32_f16 v[50:53], v[152:155], v[168:171], v[50:53]
	v_mfma_f32_16x16x32_f16 v[46:49], v[160:163], v[78:81], v[46:49]
	v_mfma_f32_16x16x32_f16 v[42:45], v[160:163], v[168:171], v[42:45]
	v_mfma_f32_16x16x32_f16 v[140:143], v[152:155], v[78:81], v[62:65]
	s_setprio 0
	s_barrier
	s_nop 1
	ds_read_b128 v[62:65], v110 offset:12288
	ds_read_b128 v[144:147], v110 offset:13312
	ds_read_b128 v[148:151], v109 offset:12288
	ds_read_b128 v[152:155], v109 offset:13312
	ds_read_b128 v[156:159], v108 offset:12288
	ds_read_b128 v[160:163], v108 offset:13312
	s_waitcnt vmcnt(4)
	s_barrier
	s_waitcnt lgkmcnt(0)
	s_setprio 1
	s_waitcnt lgkmcnt(0)
	v_mfma_f32_16x16x32_f16 v[38:41], v[62:65], v[118:121], v[38:41]
	v_mfma_f32_16x16x32_f16 v[34:37], v[62:65], v[132:135], v[34:37]
	v_mfma_f32_16x16x32_f16 v[30:33], v[148:151], v[118:121], v[30:33]
	v_mfma_f32_16x16x32_f16 v[26:29], v[148:151], v[132:135], v[26:29]
	v_mfma_f32_16x16x32_f16 v[22:25], v[156:159], v[118:121], v[22:25]
	v_mfma_f32_16x16x32_f16 v[18:21], v[156:159], v[132:135], v[18:21]
	v_mfma_f32_16x16x32_f16 v[38:41], v[144:147], v[128:131], v[38:41]
	v_mfma_f32_16x16x32_f16 v[34:37], v[144:147], v[136:139], v[34:37]
	v_mfma_f32_16x16x32_f16 v[30:33], v[152:155], v[128:131], v[30:33]
	v_mfma_f32_16x16x32_f16 v[26:29], v[152:155], v[136:139], v[26:29]
	v_mfma_f32_16x16x32_f16 v[22:25], v[160:163], v[128:131], v[22:25]
	v_mfma_f32_16x16x32_f16 v[18:21], v[160:163], v[136:139], v[18:21]
	s_setprio 0
	s_setprio 1
	v_mfma_f32_16x16x32_f16 v[10:13], v[62:65], v[98:101], v[10:13]
	v_mfma_f32_16x16x32_f16 v[128:131], v[144:147], v[168:171], v[10:13]
	v_mfma_f32_16x16x32_f16 v[6:9], v[148:151], v[74:77], v[6:9]
	v_mfma_f32_16x16x32_f16 v[2:5], v[148:151], v[98:101], v[2:5]
	v_mfma_f32_16x16x32_f16 v[10:13], v[156:159], v[74:77], v[54:57]
	v_mfma_f32_16x16x32_f16 v[14:17], v[62:65], v[74:77], v[14:17]
	v_mfma_f32_16x16x32_f16 v[6:9], v[152:155], v[78:81], v[6:9]
	v_mfma_f32_16x16x32_f16 v[2:5], v[152:155], v[168:171], v[2:5]
	v_mfma_f32_16x16x32_f16 v[132:135], v[160:163], v[78:81], v[10:13]
	v_mfma_f32_16x16x32_f16 v[10:13], v[156:159], v[98:101], v[58:61]
	v_mfma_f32_16x16x32_f16 v[118:121], v[144:147], v[78:81], v[14:17]
	v_mfma_f32_16x16x32_f16 v[136:139], v[160:163], v[168:171], v[10:13]
	s_setprio 0
	s_barrier
	s_nop 3
	ds_read_b128 v[10:13], v117
	ds_read_b128 v[14:17], v117 offset:1024
	ds_read_b128 v[144:147], v117 offset:2048
	ds_read_b128 v[148:151], v117 offset:3072
	ds_read_b128 v[54:57], v110 offset:24576
	ds_read_b128 v[152:155], v110 offset:25600
	ds_read_b128 v[156:159], v109 offset:24576
	ds_read_b128 v[160:163], v109 offset:25600
	ds_read_b128 v[168:171], v108 offset:24576
	ds_read_b128 v[172:175], v108 offset:25600
	s_waitcnt vmcnt(2)
	s_barrier
	s_waitcnt lgkmcnt(0)
	s_setprio 1
	s_waitcnt lgkmcnt(0)
	v_mfma_f32_16x16x32_f16 v[58:61], v[54:57], v[10:13], v[94:97]
	v_mfma_f32_16x16x32_f16 v[98:101], v[152:155], v[14:17], v[58:61]
	v_mfma_f32_16x16x32_f16 v[58:61], v[54:57], v[144:147], v[90:93]
	v_mfma_f32_16x16x32_f16 v[90:93], v[152:155], v[148:151], v[58:61]
	v_mfma_f32_16x16x32_f16 v[58:61], v[156:159], v[10:13], v[86:89]
	v_mfma_f32_16x16x32_f16 v[78:81], v[160:163], v[14:17], v[58:61]
	v_mfma_f32_16x16x32_f16 v[58:61], v[156:159], v[144:147], v[82:85]
	v_mfma_f32_16x16x32_f16 v[74:77], v[160:163], v[148:151], v[58:61]
	v_mfma_f32_16x16x32_f16 v[58:61], v[168:171], v[10:13], v[124:127]
	v_mfma_f32_16x16x32_f16 v[62:65], v[172:175], v[14:17], v[58:61]
	v_mfma_f32_16x16x32_f16 v[58:61], v[168:171], v[144:147], v[164:167]
	v_mfma_f32_16x16x32_f16 v[58:61], v[172:175], v[148:151], v[58:61]
	s_setprio 0
	s_barrier
	ds_read_b128 v[94:97], v114
	ds_read_b128 v[122:125], v114 offset:1024
	ds_read_b128 v[164:167], v114 offset:2048
	ds_read_b128 v[112:115], v114 offset:3072
	s_waitcnt vmcnt(0)
	s_barrier
	s_waitcnt lgkmcnt(0)
	s_setprio 1
	s_waitcnt lgkmcnt(0)
	v_mfma_f32_16x16x32_f16 v[70:73], v[54:57], v[94:97], v[70:73]
	v_mfma_f32_16x16x32_f16 v[54:57], v[54:57], v[164:167], v[66:69]
	v_mfma_f32_16x16x32_f16 v[82:85], v[152:155], v[112:115], v[54:57]
	v_mfma_f32_16x16x32_f16 v[54:57], v[156:159], v[94:97], v[140:143]
	v_mfma_f32_16x16x32_f16 v[50:53], v[156:159], v[164:167], v[50:53]
	v_mfma_f32_16x16x32_f16 v[46:49], v[168:171], v[94:97], v[46:49]
	v_mfma_f32_16x16x32_f16 v[42:45], v[168:171], v[164:167], v[42:45]
	v_mfma_f32_16x16x32_f16 v[86:89], v[152:155], v[122:125], v[70:73]
	v_mfma_f32_16x16x32_f16 v[70:73], v[160:163], v[122:125], v[54:57]
	v_mfma_f32_16x16x32_f16 v[66:69], v[160:163], v[112:115], v[50:53]
	v_mfma_f32_16x16x32_f16 v[54:57], v[172:175], v[122:125], v[46:49]
	v_mfma_f32_16x16x32_f16 v[50:53], v[172:175], v[112:115], v[42:45]
	s_setprio 0
	s_barrier
	ds_read_b128 v[140:143], v110 offset:36864
	ds_read_b128 v[152:155], v110 offset:37888
	ds_read_b128 v[156:159], v109 offset:36864
	ds_read_b128 v[160:163], v109 offset:37888
	ds_read_b128 v[168:171], v108 offset:36864
	ds_read_b128 v[106:109], v108 offset:37888
	s_barrier
	s_waitcnt lgkmcnt(0)
	s_setprio 1
	s_waitcnt lgkmcnt(0)
	v_mfma_f32_16x16x32_f16 v[38:41], v[140:143], v[10:13], v[38:41]
	v_mfma_f32_16x16x32_f16 v[30:33], v[156:159], v[10:13], v[30:33]
	v_mfma_f32_16x16x32_f16 v[10:13], v[168:171], v[10:13], v[22:25]
	v_mfma_f32_16x16x32_f16 v[46:49], v[152:155], v[14:17], v[38:41]
	v_mfma_f32_16x16x32_f16 v[34:37], v[140:143], v[144:147], v[34:37]
	v_mfma_f32_16x16x32_f16 v[30:33], v[160:163], v[14:17], v[30:33]
	v_mfma_f32_16x16x32_f16 v[26:29], v[156:159], v[144:147], v[26:29]
	v_mfma_f32_16x16x32_f16 v[14:17], v[106:109], v[14:17], v[10:13]
	v_mfma_f32_16x16x32_f16 v[10:13], v[168:171], v[144:147], v[18:21]
	v_mfma_f32_16x16x32_f16 v[42:45], v[152:155], v[148:151], v[34:37]
	v_mfma_f32_16x16x32_f16 v[26:29], v[160:163], v[148:151], v[26:29]
	v_mfma_f32_16x16x32_f16 v[10:13], v[106:109], v[148:151], v[10:13]
	s_setprio 0
	s_setprio 1
	v_mfma_f32_16x16x32_f16 v[18:21], v[140:143], v[94:97], v[118:121]
	v_mfma_f32_16x16x32_f16 v[38:41], v[152:155], v[122:125], v[18:21]
	v_mfma_f32_16x16x32_f16 v[18:21], v[140:143], v[164:167], v[128:131]
	v_mfma_f32_16x16x32_f16 v[2:5], v[156:159], v[164:167], v[2:5]
	v_mfma_f32_16x16x32_f16 v[34:37], v[152:155], v[112:115], v[18:21]
	v_mfma_f32_16x16x32_f16 v[6:9], v[156:159], v[94:97], v[6:9]
	v_mfma_f32_16x16x32_f16 v[18:21], v[160:163], v[112:115], v[2:5]
	v_mfma_f32_16x16x32_f16 v[2:5], v[168:171], v[94:97], v[132:135]
	v_mfma_f32_16x16x32_f16 v[22:25], v[160:163], v[122:125], v[6:9]
	v_mfma_f32_16x16x32_f16 v[6:9], v[106:109], v[122:125], v[2:5]
	v_mfma_f32_16x16x32_f16 v[2:5], v[168:171], v[164:167], v[136:139]
	v_mfma_f32_16x16x32_f16 v[2:5], v[106:109], v[112:115], v[2:5]
	s_setprio 0
	s_andn2_b64 vcc, exec, vcc
	s_barrier
	s_cbranch_vccnz .LBB1_6
	s_barrier
